# layer-1 weight conversion (hand-written tile routine) overlapped with layer-0 MoE up/down GEMM phases: half the workgroups convert before their units, half after
# speedup vs baseline: 1.0139x; 1.0139x over previous
; #define LAS __attribute__((address_space(3)))
; __device__ __forceinline__ int lane_id_v() { int l; asm volatile("v_mbcnt_lo_u32_b32 %0, -1, 0\n\tv_mbcnt_hi_u32_b32 %0, -1, %0" : "=v"(l)); return l; }
; __global__ void __launch_bounds__(NTHR, 2) mega_fwd(Args args) {
;     extern __shared__ __attribute__((aligned(16))) unsigned char lds_raw[];
;     Frame F;
;     F.lds = (LAS unsigned char*)lds_raw; F.MISC = (volatile LAS unsigned*)(F.lds + MISC_OFF);
;     F.wave = __builtin_amdgcn_readfirstlane((int)threadIdx.x >> 6); F.lane = lane_id_v(); F.tid = F.wave * 64 + F.lane;
;     F.G = gridDim.x; { const int bx = blockIdx.x; const int vcu = (F.G % 8 == 0) ? (bx % 8) * (F.G / 8) + bx / 8 : bx; F.gw = vcu * NWAVES + F.wave; F.NGW = F.G * NWAVES; }
_ZN2mk8mega_fwdENS_4ArgsE:
	v_mbcnt_lo_u32_b32 v64, -1, 0
	v_mbcnt_hi_u32_b32 v64, -1, v64
	s_mov_b32 s101, 0
	s_load_dword s68, s[0:1], 0xf0
	s_mov_b64 s[92:93], s[0:1]
	s_add_u32 s0, s92, 0xf0
	s_addc_u32 s1, s93, 0
	v_readfirstlane_b32 s3, v0
	v_writelane_b32 v251, s0, 0
	s_mov_b32 s10, s2
	s_nop 0
	v_writelane_b32 v251, s1, 1
	s_waitcnt lgkmcnt(0)
	s_and_b32 s0, s68, 7
	s_cmp_lg_u32 s0, 0
	s_cbranch_scc1 .LBB0_2
	s_ashr_i32 s1, s2, 31
	s_lshr_b32 s1, s1, 29
	s_add_i32 s1, s2, s1
	s_and_b32 s4, s1, -8
	s_ashr_i32 s0, s68, 3
	s_sub_i32 s4, s2, s4
	s_mul_i32 s0, s0, s4
	s_ashr_i32 s1, s1, 3
	s_add_i32 s10, s0, s1

; #define INL(j) (((MK_PHMASK >> (j)) & 1) && INR(pb + (j)))
; __device__ __forceinline__ void wg_convert_layer(Frame& F, int l) {
;     __syncthreads();
;     for (int it = F.gw >> 3; it < WG_ITEMS_PER_LAYER; it += F.G) wg_conv_item(F, l, it);
; }
; __global__ void __launch_bounds__(NTHR, 2) mega_fwd(Args args) {
;     ...
;         if (INL(0)) { if (l == 1) wg_convert_layer(F, 1);
.LBB0_290:
	s_andn2_b64 vcc, exec, s[4:5]
	s_cbranch_vccnz .LBB0_450
	v_readlane_b32 s16, v248, 1
	s_ashr_i32 s50, s76, 3
	s_addk_i32 s50, 0x800
	v_readlane_b32 s17, v248, 2
	s_cmpk_gt_i32 s50, 0x80f
	v_readlane_b32 s0, v250, 10
	v_readlane_b32 s1, v251, 11
	v_readlane_b32 s15, v251, 12
	v_readlane_b32 s17, v251, 13
	s_mov_b32 s67, 0x8002000
	s_barrier
	s_cbranch_scc1 .LBB0_445
	s_add_u32 s51, s44, 0x1c500000
	s_addc_u32 s58, s45, 0
	s_add_u32 s59, s44, 0x10500000
	s_addc_u32 s60, s45, 0
	s_add_u32 s61, s44, 0x1b00000
	s_addc_u32 s62, s45, 0
	s_lshl_b32 s4, s50, 5
	s_lshl_b32 s63, s50, 8
	s_lshl_b32 s64, s16, 8
	s_add_i32 s65, s4, 0xffffe600
	s_lshl_b32 s66, s16, 5
	s_branch .LBB0_294

; __device__ __forceinline__ int moe_t1(int NT, int G) { const int t1 = NT < G / 4 ? NT : G / 4; return (4 * (NT - t1) < G / 2) ? t1 : NT; }
; #define INL(j) (((MK_PHMASK >> (j)) & 1) && INR(pb + (j)))
; __global__ void __launch_bounds__(NTHR, 2) mega_fwd(Args args) {
;     ...
;         for (int sp = 0; sp < 3; ++sp) {
;             if (INL(10 + sp)) {
;                 if (sp == 0) moe_tables(F, l);
;                 const int NT = (int)F.MISC[MT_NT], T1 = moe_t1(NT, F.G), nUW = 4 * (NT - T1), nUR = (nUW + 7) & ~7;
;                 const bool doUp = sp == 0 || (sp == 1 && bx < nUW), doDown = (sp == 1 && bx >= nUR) || sp == 2;
;                 if (doUp) {
.LBB0_1552:
	s_cmp_ge_u32 s101, 8
	s_cbranch_scc1 .Lcv_ret_top
	v_readlane_b32 s100, v251, 3
	s_nop 3
	s_bitcmp1_b32 s100, 3
	s_cbranch_scc1 .Lcv_ret_top
	s_mov_b32 s100, 0
	s_branch .Lcv_run

; #define SEAM(k) do { if (INR(k) && INR((k) + 1)) xcd_barrier(bar); F.lane = lane_id_v(); F.tid = F.wave * 64 + F.lane; { int z_; asm volatile("s_mov_b32 %0, 0" : "=s"(z_)); F.ws = args.ws + z_; F.out = args.out + z_; F.ctl = (gu32*)(args.ws + WS_CTL) + z_; F.in = args.in + z_; F.gw = gw0 + z_; } } while (0)
; __device__ __forceinline__ void xcd_barrier(const XcdBarrier& b) {
;     asm volatile("s_waitcnt vmcnt(0)" ::: "memory");
;     __syncthreads();
;     if (threadIdx.x == 0) {
;         unsigned* bar = b.bar;
;         __builtin_amdgcn_s_waitcnt(0);
;         unsigned nloc = b.st[0], nx = b.st[1];
;         if (nloc == 0u) { xcd_barrier_complete(bar, b.x, nloc, nx); b.st[0] = nloc; b.st[1] = nx; }
; __global__ void __launch_bounds__(NTHR, 2) mega_fwd(Args args) {
;     ...
;             SEAM(pb + 10 + sp);
.LBB0_1642:
	s_add_i32 s94, s94, 1
	s_cmp_lt_i32 s94, s75
	s_cselect_b64 s[4:5], -1, 0
	s_and_b64 s[4:5], s[70:71], s[4:5]
	s_andn2_b64 vcc, exec, s[4:5]
	s_cbranch_vccnz .LBB0_1551
	s_cmp_ge_u32 s101, 8
	s_cbranch_scc1 .Lcv_ret_bot
	v_readlane_b32 s100, v251, 3
	s_nop 3
	s_bitcmp1_b32 s100, 3
	s_cbranch_scc0 .Lcv_ret_bot
	s_mov_b32 s100, 1
	s_branch .Lcv_run
.Lcv_ret_bot:
	s_waitcnt vmcnt(0)
	s_waitcnt vmcnt(0) lgkmcnt(0)
	s_barrier
	s_and_saveexec_b64 s[4:5], s[72:73]
	s_cbranch_execz .LBB0_1550
	v_readlane_b32 s6, v249, 58
	s_waitcnt vmcnt(0) expcnt(0) lgkmcnt(0)
	s_nop 0
	v_mov_b32_e32 v0, s6
	ds_read_b32 v3, v0
	v_readlane_b32 s6, v249, 59
	s_waitcnt lgkmcnt(0)
	v_cmp_ne_u32_e32 vcc, 0, v3
	v_mov_b32_e32 v0, s6
	ds_read_b32 v2, v0
	s_cbranch_vccnz .LBB0_1659
	v_readlane_b32 s8, v251, 0
	v_readlane_b32 s9, v251, 1
	s_load_dwordx2 s[6:7], s[8:9], 0x4
	s_waitcnt lgkmcnt(0)
	s_mul_i32 s6, s6, s68
	s_mul_i32 s6, s6, s7
	s_mov_b32 s7, 1
	s_branch .LBB0_1647

; #define LAS __attribute__((address_space(3)))
; __device__ __forceinline__ int lane_id_v() { int l; asm volatile("v_mbcnt_lo_u32_b32 %0, -1, 0\n\tv_mbcnt_hi_u32_b32 %0, -1, %0" : "=v"(l)); return l; }
; __device__ __forceinline__ void wg_convert_tile(Frame& F, const float* W, int ldw, bf16_t* WT, int Kd, int k0, int n0, int kind, const float* kgain) {
;     const int lane = lane_id_v(), w = F.wave;
;     LAS unsigned char* img = F.lds;
;     const float* src = W + (size_t)(k0 + 8 * w) * ldw + n0 + 4 * lane;
;     f32x4 ld[2][8];
; #pragma unroll
;     for (int j = 0; j < 8; ++j) ld[0][j] = __builtin_nontemporal_load((const f32x4*)(src + (size_t)j * ldw));
; #pragma unroll
;     for (int p = 0; p < 4; ++p) {
;         if (p < 3) {
; #pragma unroll
;             for (int j = 0; j < 8; ++j) ld[(p + 1) & 1][j] = __builtin_nontemporal_load((const f32x4*)(src + (size_t)(64 * (p + 1) + j) * ldw)); }
;         float g[8];
; #pragma unroll
;         for (int j = 0; j < 8; ++j) g[j] = kgain ? kgain[k0 + 64 * p + 8 * w + j] : 1.f;
; __device__ __forceinline__ void wg_conv_item(Frame& F, int l, int it) {
;     if (it < 208) { const int kt = it / 26, nt = it % 26;
;         wg_convert_tile(F, F.in[3] + (size_t)l * D * INW, INW, WSP(bf16_t, WS_WIN + l * SZ_WIN), D, 256 * kt, 256 * nt, -1, nullptr); return; }
;     it -= 208;
;     if (it < 320) { const int which = it / 64, rr = it % 64, kt = rr / 8, nt = rr % 8;
;         const int src = which == 0 ? 10 : 12 + which;
;         const size_t dst = which == 0 ? WS_WOUT : (which == 1 ? WS_WCQ : (which == 2 ? WS_WCK : (which == 3 ? WS_WCV : WS_WCO)));
;         wg_convert_tile(F, F.in[src] + (size_t)l * D * D, D, WSP(bf16_t, dst + l * SZ_SQ), D, 256 * kt, 256 * nt, -1, which == 1 ? F.in[11] + l * D : nullptr); return; }
;     it -= 320;
;     const int e = it / 48, rr = it % 48, kind = rr / 16, item = rr % 16;
;     if (kind < 2) { const int kt = item / 2, nt = item % 2;
;         wg_convert_tile(F, F.in[24 + kind] + ((size_t)l * NE + e) * D * FH, FH, WSP(bf16_t, WS_W13 + l * SZ_W13) + (size_t)e * 1024 * D, D, 256 * kt, 256 * nt, kind, F.in[19] + l * D); }
;     else { const int kt = item / 8, nt = item % 8;
;         wg_convert_tile(F, F.in[26] + ((size_t)l * NE + e) * FH * D, D, WSP(bf16_t, WS_W2 + l * SZ_W2) + (size_t)e * D * FH, FH, 256 * kt, 256 * nt, -1, nullptr); }
; }
.Lcv_run:
	v_writelane_b32 v253, s6, 0
	v_writelane_b32 v253, s7, 1
	v_writelane_b32 v253, s8, 2
	v_writelane_b32 v253, s9, 3
	v_writelane_b32 v253, s11, 4
	v_writelane_b32 v253, s12, 5
	v_writelane_b32 v253, s13, 6
	v_writelane_b32 v253, s14, 7
	v_writelane_b32 v253, s32, 8
	v_writelane_b32 v253, s38, 9
	v_writelane_b32 v253, s39, 10
	v_writelane_b32 v253, s55, 11
	v_writelane_b32 v253, s56, 12
	v_writelane_b32 v253, s57, 13
	v_writelane_b32 v253, s58, 14
	v_writelane_b32 v253, s59, 15
	v_writelane_b32 v253, s60, 16
	v_writelane_b32 v253, s61, 17
	v_writelane_b32 v253, s62, 18
	v_writelane_b32 v253, s63, 19
	v_writelane_b32 v253, s64, 20
	v_writelane_b32 v253, s65, 21
	v_writelane_b32 v253, s67, 22
	v_writelane_b32 v253, s70, 23
	v_writelane_b32 v253, s71, 24
	v_writelane_b32 v253, s76, 25
	v_writelane_b32 v253, s80, 26
	v_writelane_b32 v253, s81, 27
	v_writelane_b32 v253, s83, 28
	v_writelane_b32 v253, s95, 29
	v_writelane_b32 v253, s96, 30
	v_writelane_b32 v253, s97, 31
	v_writelane_b32 v253, s98, 32
	v_writelane_b32 v253, s99, 33
	v_readlane_b32 s6, v251, 9
	v_readlane_b32 s7, v251, 10
	v_readlane_b32 s8, v251, 2
	v_readlane_b32 s9, v251, 3
	v_mbcnt_lo_u32_b32 v2, -1, 0
	v_mbcnt_hi_u32_b32 v2, -1, v2
	s_nop 3
	s_lshr_b32 s9, s9, 3
	s_load_dwordx2 s[12:13], s[6:7], 0xe0
	v_lshlrev_b32_e32 v3, 4, v2
	v_and_b32_e32 v14, 31, v2
	v_lshrrev_b32_e32 v15, 5, v2
	v_lshl_add_u32 v16, s8, 1, v15
	v_mov_b32_e32 v17, 0
	s_mov_b32 s11, 4
	s_waitcnt lgkmcnt(0)
.Lcv_item:
	s_lshl_b32 s14, s101, 8
	s_add_i32 s14, s14, s9
	s_mov_b32 s67, 0
	s_mov_b64 s[70:71], 0
	s_movk_i32 s55, 0x1000
	s_cmpk_lt_u32 s14, 0xd0
	s_cbranch_scc1 .Lcv_A
	s_cmpk_lt_u32 s14, 0x210
	s_cbranch_scc1 .Lcv_B
	s_sub_i32 s76, s14, 0x210
	s_mul_i32 s83, s76, 0xaaab
	s_lshr_b32 s83, s83, 21
	s_mul_i32 s95, s83, 48
	s_sub_i32 s76, s76, s95
	s_lshr_b32 s95, s76, 4
	s_and_b32 s76, s76, 15
	s_add_i32 s99, s83, 32
	s_lshl_b32 s99, s99, 22
	s_cmp_eq_u32 s95, 2
	s_cbranch_scc1 .Lcv_C2
	s_lshl_b32 s98, s95, 3
	s_addk_i32 s98, 0xc0
	s_load_dwordx2 s[96:97], s[6:7], s98 offset:0x0
	s_load_dwordx2 s[70:71], s[6:7], 0x98
	s_lshr_b32 s98, s76, 1
	s_and_b32 s76, s76, 1
	s_lshl_b32 s14, s98, 19
	s_add_u32 s99, s99, s14
	s_lshl_b32 s14, s76, 10
	s_add_u32 s99, s99, s14
	s_movk_i32 s32, 0x800
	s_lshl_b32 s14, s83, 22
	s_add_u32 s14, s14, 0x10500000
	s_lshl_b32 s76, s76, 21
	s_add_u32 s14, s14, s76
	s_lshl_b32 s95, s95, 19
	s_add_u32 s14, s14, s95
	s_lshl_b32 s76, s98, 9
	s_add_u32 s95, s14, s76
	s_mov_b32 s76, s98
	s_mov_b32 s67, 1
	s_waitcnt lgkmcnt(0)
	s_add_u32 s70, s70, 0x2000
	s_addc_u32 s71, s71, 0
	s_branch .Lcv_go
.Lcv_C2:
	s_load_dwordx2 s[96:97], s[6:7], 0xd0
	s_lshr_b32 s98, s76, 3
	s_and_b32 s76, s76, 7
	s_lshl_b32 s14, s98, 21
	s_add_u32 s99, s99, s14
	s_lshl_b32 s14, s76, 10
	s_add_u32 s99, s99, s14
	s_movk_i32 s32, 0x2000
	s_lshl_b32 s14, s83, 21
	s_add_u32 s14, s14, 0x1c500000
	s_lshl_b32 s76, s76, 18
	s_add_u32 s14, s14, s76
	s_lshl_b32 s76, s98, 9
	s_add_u32 s95, s14, s76
	s_mov_b32 s76, s98
	s_movk_i32 s55, 0x400
	s_waitcnt lgkmcnt(0)
	s_branch .Lcv_go
.Lcv_A:
	s_load_dwordx2 s[96:97], s[6:7], 0x18
	s_mul_i32 s76, s14, 0x9d9
	s_lshr_b32 s76, s76, 16
	s_mul_i32 s83, s76, 26
	s_sub_i32 s83, s14, s83
	s_mul_i32 s99, s76, 0x682000
	s_lshl_b32 s14, s83, 10
	s_add_u32 s99, s99, s14
	s_add_u32 s99, s99, 0x3410000
	s_movk_i32 s32, 0x6820
	s_lshl_b32 s95, s83, 20
	s_add_u32 s95, s95, 0x1b00000
	s_lshl_b32 s14, s76, 9
	s_add_u32 s95, s95, s14
	s_waitcnt lgkmcnt(0)
	s_branch .Lcv_go
.Lcv_B:
	s_sub_i32 s76, s14, 0xd0
	s_lshr_b32 s83, s76, 6
	s_and_b32 s76, s76, 63
	s_lshl_b32 s98, s83, 3
	s_addk_i32 s98, 0x60
	s_cmp_eq_u32 s83, 0
	s_cselect_b32 s98, 0x50, s98
	s_load_dwordx2 s[96:97], s[6:7], s98 offset:0x0
	s_cmp_eq_u32 s83, 1
	s_cbranch_scc0 .Lcv_B_nogain
	s_load_dwordx2 s[70:71], s[6:7], 0x58
	s_waitcnt lgkmcnt(0)
	s_add_u32 s70, s70, 0x2000
	s_addc_u32 s71, s71, 0
.Lcv_B_nogain:
	s_and_b32 s14, s76, 7
	s_lshr_b32 s76, s76, 3
	s_lshl_b32 s99, s76, 21
	s_lshl_b32 s98, s14, 10
	s_add_u32 s99, s99, s98
	s_add_u32 s99, s99, 0x1000000
	s_movk_i32 s32, 0x2000
	s_lshl_b32 s95, s83, 24
	s_add_u32 s95, s95, 0x3d00000
	s_lshl_b32 s14, s14, 20
	s_add_u32 s95, s95, s14
	s_lshl_b32 s14, s76, 9
	s_add_u32 s95, s95, s14
	s_waitcnt lgkmcnt(0)
.Lcv_go:
	s_add_u32 s38, s96, s99
	s_addc_u32 s39, s97, 0
	s_mul_i32 s98, s8, s32
	s_lshl_b32 s98, s98, 3
	s_add_u32 s38, s38, s98
	s_addc_u32 s39, s39, 0
	s_add_u32 s64, s12, s95
	s_addc_u32 s65, s13, 0
	v_mul_lo_u32 v6, v16, s55
	v_lshl_add_u32 v6, v14, 4, v6
	v_mov_b32_e32 v164, 1.0
	v_mov_b32_e32 v165, 1.0
	v_mov_b32_e32 v166, 1.0
	v_mov_b32_e32 v167, 1.0
	v_mov_b32_e32 v168, 1.0
	v_mov_b32_e32 v169, 1.0
	v_mov_b32_e32 v170, 1.0
	v_mov_b32_e32 v171, 1.0
	v_mov_b32_e32 v172, 1.0
	v_mov_b32_e32 v173, 1.0
	v_mov_b32_e32 v174, 1.0
	v_mov_b32_e32 v175, 1.0
	v_mov_b32_e32 v176, 1.0
	v_mov_b32_e32 v177, 1.0
	v_mov_b32_e32 v178, 1.0
	v_mov_b32_e32 v179, 1.0
	v_mov_b32_e32 v180, 1.0
	v_mov_b32_e32 v181, 1.0
	v_mov_b32_e32 v182, 1.0
	v_mov_b32_e32 v183, 1.0
	v_mov_b32_e32 v184, 1.0
	v_mov_b32_e32 v185, 1.0
	v_mov_b32_e32 v186, 1.0
	v_mov_b32_e32 v187, 1.0
	v_mov_b32_e32 v188, 1.0
	v_mov_b32_e32 v189, 1.0
	v_mov_b32_e32 v190, 1.0
	v_mov_b32_e32 v191, 1.0
	v_mov_b32_e32 v192, 1.0
	v_mov_b32_e32 v193, 1.0
	v_mov_b32_e32 v194, 1.0
	v_mov_b32_e32 v195, 1.0
	s_cmp_eq_u64 s[70:71], 0
	s_cbranch_scc1 .Lcv_nogain
	s_lshl_b32 s98, s76, 10
	s_lshl_b32 s99, s8, 5
	s_add_u32 s98, s98, s99
	s_add_u32 s70, s70, s98
	s_addc_u32 s71, s71, 0
	global_load_dwordx4 v[164:167], v17, s[70:71] offset:0
	global_load_dwordx4 v[168:171], v17, s[70:71] offset:16
	global_load_dwordx4 v[172:175], v17, s[70:71] offset:256
	global_load_dwordx4 v[176:179], v17, s[70:71] offset:272
	global_load_dwordx4 v[180:183], v17, s[70:71] offset:512
	global_load_dwordx4 v[184:187], v17, s[70:71] offset:528
	global_load_dwordx4 v[188:191], v17, s[70:71] offset:768
	global_load_dwordx4 v[192:195], v17, s[70:71] offset:784
; #define LAS __attribute__((address_space(3)))
; #define SB() __builtin_amdgcn_sched_barrier(0)
; __device__ __forceinline__ unsigned cvt_pk_bf16(float lo, float hi) { unsigned r; asm volatile("v_cvt_pk_bf16_f32 %0, %1, %2" : "=v"(r) : "v"(lo), "v"(hi)); return r; }
; __device__ __forceinline__ void wg_convert_tile(Frame& F, const float* W, int ldw, bf16_t* WT, int Kd, int k0, int n0, int kind, const float* kgain) {
;     ...
;     f32x4 ld[2][8];
; #pragma unroll
;     for (int j = 0; j < 8; ++j) ld[0][j] = __builtin_nontemporal_load((const f32x4*)(src + (size_t)j * ldw));
; #pragma unroll
;     for (int p = 0; p < 4; ++p) {
;         if (p < 3) {
; #pragma unroll
;             for (int j = 0; j < 8; ++j) ld[(p + 1) & 1][j] = __builtin_nontemporal_load((const f32x4*)(src + (size_t)(64 * (p + 1) + j) * ldw)); }
;         float g[8];
; #pragma unroll
;         for (int j = 0; j < 8; ++j) g[j] = kgain ? kgain[k0 + 64 * p + 8 * w + j] : 1.f;
;         SB();
;         const unsigned kc = (unsigned)(8 * p + w);
; #pragma unroll
;         for (int c = 0; c < 4; ++c) { const int n = 4 * lane + c;
;             u32x4 o; o.x = cvt_pk_bf16(ld[p & 1][0][c] * g[0], ld[p & 1][1][c] * g[1]); o.y = cvt_pk_bf16(ld[p & 1][2][c] * g[2], ld[p & 1][3][c] * g[3]);
;                      o.z = cvt_pk_bf16(ld[p & 1][4][c] * g[4], ld[p & 1][5][c] * g[5]); o.w = cvt_pk_bf16(ld[p & 1][6][c] * g[6], ld[p & 1][7][c] * g[7]);
;             *(LAS u32x4*)(img + n * 512 + ((kc ^ (unsigned)(lane & 31)) << 4)) = o; }
;         SB();
;     }
.Lcv_nogain:
	s_barrier
	s_mov_b64 s[80:81], s[38:39]
	s_mul_i32 s98, s32, 56
	global_load_dwordx4 v[100:103], v3, s[80:81] nt
	s_add_u32 s80, s80, s32
	s_addc_u32 s81, s81, 0
	global_load_dwordx4 v[104:107], v3, s[80:81] nt
	s_add_u32 s80, s80, s32
	s_addc_u32 s81, s81, 0
	global_load_dwordx4 v[108:111], v3, s[80:81] nt
	s_add_u32 s80, s80, s32
	s_addc_u32 s81, s81, 0
	global_load_dwordx4 v[112:115], v3, s[80:81] nt
	s_add_u32 s80, s80, s32
	s_addc_u32 s81, s81, 0
	global_load_dwordx4 v[116:119], v3, s[80:81] nt
	s_add_u32 s80, s80, s32
	s_addc_u32 s81, s81, 0
	global_load_dwordx4 v[120:123], v3, s[80:81] nt
	s_add_u32 s80, s80, s32
	s_addc_u32 s81, s81, 0
	global_load_dwordx4 v[124:127], v3, s[80:81] nt
	s_add_u32 s80, s80, s32
	s_addc_u32 s81, s81, 0
	global_load_dwordx4 v[128:131], v3, s[80:81] nt
	s_add_u32 s80, s80, s32
	s_addc_u32 s81, s81, 0
	s_add_u32 s80, s80, s98
	s_addc_u32 s81, s81, 0
	global_load_dwordx4 v[132:135], v3, s[80:81] nt
	s_add_u32 s80, s80, s32
	s_addc_u32 s81, s81, 0
	global_load_dwordx4 v[136:139], v3, s[80:81] nt
	s_add_u32 s80, s80, s32
	s_addc_u32 s81, s81, 0
	global_load_dwordx4 v[140:143], v3, s[80:81] nt
	s_add_u32 s80, s80, s32
	s_addc_u32 s81, s81, 0
	global_load_dwordx4 v[144:147], v3, s[80:81] nt
	s_add_u32 s80, s80, s32
	s_addc_u32 s81, s81, 0
	global_load_dwordx4 v[148:151], v3, s[80:81] nt
	s_add_u32 s80, s80, s32
	s_addc_u32 s81, s81, 0
	global_load_dwordx4 v[152:155], v3, s[80:81] nt
	s_add_u32 s80, s80, s32
	s_addc_u32 s81, s81, 0
	global_load_dwordx4 v[156:159], v3, s[80:81] nt
	s_add_u32 s80, s80, s32
	s_addc_u32 s81, s81, 0
	global_load_dwordx4 v[160:163], v3, s[80:81] nt
	s_add_u32 s80, s80, s32
	s_addc_u32 s81, s81, 0
	s_add_u32 s80, s80, s98
	s_addc_u32 s81, s81, 0
	s_waitcnt vmcnt(8)
	s_add_i32 s99, s8, 0
	v_xor_b32_e32 v5, s99, v14
	v_lshlrev_b32_e32 v5, 4, v5
	v_lshl_add_u32 v5, v2, 11, v5
	v_mul_f32_e32 v12, v164, v100
	v_mul_f32_e32 v13, v165, v104
	v_cvt_pk_bf16_f32 v8, v12, v13
	v_mul_f32_e32 v12, v166, v108
	v_mul_f32_e32 v13, v167, v112
	v_cvt_pk_bf16_f32 v9, v12, v13
	v_mul_f32_e32 v12, v168, v116
	v_mul_f32_e32 v13, v169, v120
	v_cvt_pk_bf16_f32 v10, v12, v13
	v_mul_f32_e32 v12, v170, v124
	v_mul_f32_e32 v13, v171, v128
	v_cvt_pk_bf16_f32 v11, v12, v13
	ds_write_b128 v5, v[8:11]
	v_mul_f32_e32 v12, v164, v101
	v_mul_f32_e32 v13, v165, v105
	v_cvt_pk_bf16_f32 v8, v12, v13
	v_mul_f32_e32 v12, v166, v109
	v_mul_f32_e32 v13, v167, v113
	v_cvt_pk_bf16_f32 v9, v12, v13
	v_mul_f32_e32 v12, v168, v117
	v_mul_f32_e32 v13, v169, v121
	v_cvt_pk_bf16_f32 v10, v12, v13
	v_mul_f32_e32 v12, v170, v125
	v_mul_f32_e32 v13, v171, v129
	v_cvt_pk_bf16_f32 v11, v12, v13
	ds_write_b128 v5, v[8:11] offset:512
	v_mul_f32_e32 v12, v164, v102
	v_mul_f32_e32 v13, v165, v106
	v_cvt_pk_bf16_f32 v8, v12, v13
	v_mul_f32_e32 v12, v166, v110
	v_mul_f32_e32 v13, v167, v114
	v_cvt_pk_bf16_f32 v9, v12, v13
	v_mul_f32_e32 v12, v168, v118
	v_mul_f32_e32 v13, v169, v122
	v_cvt_pk_bf16_f32 v10, v12, v13
	v_mul_f32_e32 v12, v170, v126
	v_mul_f32_e32 v13, v171, v130
	v_cvt_pk_bf16_f32 v11, v12, v13
	ds_write_b128 v5, v[8:11] offset:1024
	v_mul_f32_e32 v12, v164, v103
	v_mul_f32_e32 v13, v165, v107
	v_cvt_pk_bf16_f32 v8, v12, v13
	v_mul_f32_e32 v12, v166, v111
	v_mul_f32_e32 v13, v167, v115
	v_cvt_pk_bf16_f32 v9, v12, v13
	v_mul_f32_e32 v12, v168, v119
	v_mul_f32_e32 v13, v169, v123
	v_cvt_pk_bf16_f32 v10, v12, v13
	v_mul_f32_e32 v12, v170, v127
	v_mul_f32_e32 v13, v171, v131
	v_cvt_pk_bf16_f32 v11, v12, v13
	ds_write_b128 v5, v[8:11] offset:1536
	global_load_dwordx4 v[100:103], v3, s[80:81] nt
	s_add_u32 s80, s80, s32
	s_addc_u32 s81, s81, 0
	global_load_dwordx4 v[104:107], v3, s[80:81] nt
	s_add_u32 s80, s80, s32
	s_addc_u32 s81, s81, 0
	global_load_dwordx4 v[108:111], v3, s[80:81] nt
	s_add_u32 s80, s80, s32
	s_addc_u32 s81, s81, 0
	global_load_dwordx4 v[112:115], v3, s[80:81] nt
	s_add_u32 s80, s80, s32
	s_addc_u32 s81, s81, 0
	global_load_dwordx4 v[116:119], v3, s[80:81] nt
	s_add_u32 s80, s80, s32
	s_addc_u32 s81, s81, 0
	global_load_dwordx4 v[120:123], v3, s[80:81] nt
	s_add_u32 s80, s80, s32
	s_addc_u32 s81, s81, 0
	global_load_dwordx4 v[124:127], v3, s[80:81] nt
	s_add_u32 s80, s80, s32
	s_addc_u32 s81, s81, 0
	global_load_dwordx4 v[128:131], v3, s[80:81] nt
	s_add_u32 s80, s80, s32
	s_addc_u32 s81, s81, 0
	s_add_u32 s80, s80, s98
	s_addc_u32 s81, s81, 0
	s_waitcnt vmcnt(8)
; #define LAS __attribute__((address_space(3)))
; #define SB() __builtin_amdgcn_sched_barrier(0)
; __device__ __forceinline__ unsigned cvt_pk_bf16(float lo, float hi) { unsigned r; asm volatile("v_cvt_pk_bf16_f32 %0, %1, %2" : "=v"(r) : "v"(lo), "v"(hi)); return r; }
; __device__ __forceinline__ void wg_convert_tile(Frame& F, const float* W, int ldw, bf16_t* WT, int Kd, int k0, int n0, int kind, const float* kgain) {
;     ...
; #pragma unroll
;     for (int p = 0; p < 4; ++p) {
;         if (p < 3) {
; #pragma unroll
;             for (int j = 0; j < 8; ++j) ld[(p + 1) & 1][j] = __builtin_nontemporal_load((const f32x4*)(src + (size_t)(64 * (p + 1) + j) * ldw)); }
;         float g[8];
; #pragma unroll
;         for (int j = 0; j < 8; ++j) g[j] = kgain ? kgain[k0 + 64 * p + 8 * w + j] : 1.f;
;         SB();
;         const unsigned kc = (unsigned)(8 * p + w);
; #pragma unroll
;         for (int c = 0; c < 4; ++c) { const int n = 4 * lane + c;
;             u32x4 o; o.x = cvt_pk_bf16(ld[p & 1][0][c] * g[0], ld[p & 1][1][c] * g[1]); o.y = cvt_pk_bf16(ld[p & 1][2][c] * g[2], ld[p & 1][3][c] * g[3]);
;                      o.z = cvt_pk_bf16(ld[p & 1][4][c] * g[4], ld[p & 1][5][c] * g[5]); o.w = cvt_pk_bf16(ld[p & 1][6][c] * g[6], ld[p & 1][7][c] * g[7]);
;             *(LAS u32x4*)(img + n * 512 + ((kc ^ (unsigned)(lane & 31)) << 4)) = o; }
;         SB();
;     }
	s_add_i32 s99, s8, 8
	v_xor_b32_e32 v5, s99, v14
	v_lshlrev_b32_e32 v5, 4, v5
	v_lshl_add_u32 v5, v2, 11, v5
	v_mul_f32_e32 v12, v172, v132
	v_mul_f32_e32 v13, v173, v136
	v_cvt_pk_bf16_f32 v8, v12, v13
	v_mul_f32_e32 v12, v174, v140
	v_mul_f32_e32 v13, v175, v144
	v_cvt_pk_bf16_f32 v9, v12, v13
	v_mul_f32_e32 v12, v176, v148
	v_mul_f32_e32 v13, v177, v152
	v_cvt_pk_bf16_f32 v10, v12, v13
	v_mul_f32_e32 v12, v178, v156
	v_mul_f32_e32 v13, v179, v160
	v_cvt_pk_bf16_f32 v11, v12, v13
	ds_write_b128 v5, v[8:11]
	v_mul_f32_e32 v12, v172, v133
	v_mul_f32_e32 v13, v173, v137
	v_cvt_pk_bf16_f32 v8, v12, v13
	v_mul_f32_e32 v12, v174, v141
	v_mul_f32_e32 v13, v175, v145
	v_cvt_pk_bf16_f32 v9, v12, v13
	v_mul_f32_e32 v12, v176, v149
	v_mul_f32_e32 v13, v177, v153
	v_cvt_pk_bf16_f32 v10, v12, v13
	v_mul_f32_e32 v12, v178, v157
	v_mul_f32_e32 v13, v179, v161
	v_cvt_pk_bf16_f32 v11, v12, v13
	ds_write_b128 v5, v[8:11] offset:512
	v_mul_f32_e32 v12, v172, v134
	v_mul_f32_e32 v13, v173, v138
	v_cvt_pk_bf16_f32 v8, v12, v13
	v_mul_f32_e32 v12, v174, v142
	v_mul_f32_e32 v13, v175, v146
	v_cvt_pk_bf16_f32 v9, v12, v13
	v_mul_f32_e32 v12, v176, v150
	v_mul_f32_e32 v13, v177, v154
	v_cvt_pk_bf16_f32 v10, v12, v13
	v_mul_f32_e32 v12, v178, v158
	v_mul_f32_e32 v13, v179, v162
	v_cvt_pk_bf16_f32 v11, v12, v13
	ds_write_b128 v5, v[8:11] offset:1024
	v_mul_f32_e32 v12, v172, v135
	v_mul_f32_e32 v13, v173, v139
	v_cvt_pk_bf16_f32 v8, v12, v13
	v_mul_f32_e32 v12, v174, v143
	v_mul_f32_e32 v13, v175, v147
	v_cvt_pk_bf16_f32 v9, v12, v13
	v_mul_f32_e32 v12, v176, v151
	v_mul_f32_e32 v13, v177, v155
	v_cvt_pk_bf16_f32 v10, v12, v13
	v_mul_f32_e32 v12, v178, v159
	v_mul_f32_e32 v13, v179, v163
	v_cvt_pk_bf16_f32 v11, v12, v13
	ds_write_b128 v5, v[8:11] offset:1536
	global_load_dwordx4 v[132:135], v3, s[80:81] nt
	s_add_u32 s80, s80, s32
	s_addc_u32 s81, s81, 0
	global_load_dwordx4 v[136:139], v3, s[80:81] nt
	s_add_u32 s80, s80, s32
	s_addc_u32 s81, s81, 0
	global_load_dwordx4 v[140:143], v3, s[80:81] nt
	s_add_u32 s80, s80, s32
	s_addc_u32 s81, s81, 0
	global_load_dwordx4 v[144:147], v3, s[80:81] nt
	s_add_u32 s80, s80, s32
	s_addc_u32 s81, s81, 0
	global_load_dwordx4 v[148:151], v3, s[80:81] nt
	s_add_u32 s80, s80, s32
	s_addc_u32 s81, s81, 0
	global_load_dwordx4 v[152:155], v3, s[80:81] nt
	s_add_u32 s80, s80, s32
	s_addc_u32 s81, s81, 0
	global_load_dwordx4 v[156:159], v3, s[80:81] nt
	s_add_u32 s80, s80, s32
	s_addc_u32 s81, s81, 0
	global_load_dwordx4 v[160:163], v3, s[80:81] nt
	s_add_u32 s80, s80, s32
	s_addc_u32 s81, s81, 0
	s_add_u32 s80, s80, s98
	s_addc_u32 s81, s81, 0
	s_waitcnt vmcnt(8)
	s_add_i32 s99, s8, 16
	v_xor_b32_e32 v5, s99, v14
	v_lshlrev_b32_e32 v5, 4, v5
	v_lshl_add_u32 v5, v2, 11, v5
	v_mul_f32_e32 v12, v180, v100
	v_mul_f32_e32 v13, v181, v104
	v_cvt_pk_bf16_f32 v8, v12, v13
	v_mul_f32_e32 v12, v182, v108
	v_mul_f32_e32 v13, v183, v112
	v_cvt_pk_bf16_f32 v9, v12, v13
	v_mul_f32_e32 v12, v184, v116
	v_mul_f32_e32 v13, v185, v120
	v_cvt_pk_bf16_f32 v10, v12, v13
	v_mul_f32_e32 v12, v186, v124
	v_mul_f32_e32 v13, v187, v128
	v_cvt_pk_bf16_f32 v11, v12, v13
	ds_write_b128 v5, v[8:11]
	v_mul_f32_e32 v12, v180, v101
	v_mul_f32_e32 v13, v181, v105
	v_cvt_pk_bf16_f32 v8, v12, v13
	v_mul_f32_e32 v12, v182, v109
	v_mul_f32_e32 v13, v183, v113
	v_cvt_pk_bf16_f32 v9, v12, v13
	v_mul_f32_e32 v12, v184, v117
	v_mul_f32_e32 v13, v185, v121
	v_cvt_pk_bf16_f32 v10, v12, v13
	v_mul_f32_e32 v12, v186, v125
	v_mul_f32_e32 v13, v187, v129
	v_cvt_pk_bf16_f32 v11, v12, v13
	ds_write_b128 v5, v[8:11] offset:512
	v_mul_f32_e32 v12, v180, v102
	v_mul_f32_e32 v13, v181, v106
	v_cvt_pk_bf16_f32 v8, v12, v13
	v_mul_f32_e32 v12, v182, v110
	v_mul_f32_e32 v13, v183, v114
	v_cvt_pk_bf16_f32 v9, v12, v13
	v_mul_f32_e32 v12, v184, v118
	v_mul_f32_e32 v13, v185, v122
	v_cvt_pk_bf16_f32 v10, v12, v13
	v_mul_f32_e32 v12, v186, v126
	v_mul_f32_e32 v13, v187, v130
	v_cvt_pk_bf16_f32 v11, v12, v13
	ds_write_b128 v5, v[8:11] offset:1024
	v_mul_f32_e32 v12, v180, v103
	v_mul_f32_e32 v13, v181, v107
	v_cvt_pk_bf16_f32 v8, v12, v13
	v_mul_f32_e32 v12, v182, v111
	v_mul_f32_e32 v13, v183, v115
	v_cvt_pk_bf16_f32 v9, v12, v13
	v_mul_f32_e32 v12, v184, v119
	v_mul_f32_e32 v13, v185, v123
	v_cvt_pk_bf16_f32 v10, v12, v13
	v_mul_f32_e32 v12, v186, v127
	v_mul_f32_e32 v13, v187, v131
	v_cvt_pk_bf16_f32 v11, v12, v13
	ds_write_b128 v5, v[8:11] offset:1536
	s_waitcnt vmcnt(0)
	s_add_i32 s99, s8, 24
	v_xor_b32_e32 v5, s99, v14
	v_lshlrev_b32_e32 v5, 4, v5
	v_lshl_add_u32 v5, v2, 11, v5
	v_mul_f32_e32 v12, v188, v132
	v_mul_f32_e32 v13, v189, v136
	v_cvt_pk_bf16_f32 v8, v12, v13
	v_mul_f32_e32 v12, v190, v140
	v_mul_f32_e32 v13, v191, v144
	v_cvt_pk_bf16_f32 v9, v12, v13
	v_mul_f32_e32 v12, v192, v148
	v_mul_f32_e32 v13, v193, v152
	v_cvt_pk_bf16_f32 v10, v12, v13
	v_mul_f32_e32 v12, v194, v156
	v_mul_f32_e32 v13, v195, v160
	v_cvt_pk_bf16_f32 v11, v12, v13
	ds_write_b128 v5, v[8:11]
	v_mul_f32_e32 v12, v188, v133
	v_mul_f32_e32 v13, v189, v137
	v_cvt_pk_bf16_f32 v8, v12, v13
	v_mul_f32_e32 v12, v190, v141
	v_mul_f32_e32 v13, v191, v145
	v_cvt_pk_bf16_f32 v9, v12, v13
	v_mul_f32_e32 v12, v192, v149
	v_mul_f32_e32 v13, v193, v153
	v_cvt_pk_bf16_f32 v10, v12, v13
	v_mul_f32_e32 v12, v194, v157
	v_mul_f32_e32 v13, v195, v161
	v_cvt_pk_bf16_f32 v11, v12, v13
	ds_write_b128 v5, v[8:11] offset:512
	v_mul_f32_e32 v12, v188, v134
	v_mul_f32_e32 v13, v189, v138
	v_cvt_pk_bf16_f32 v8, v12, v13
	v_mul_f32_e32 v12, v190, v142
	v_mul_f32_e32 v13, v191, v146
	v_cvt_pk_bf16_f32 v9, v12, v13
	v_mul_f32_e32 v12, v192, v150
	v_mul_f32_e32 v13, v193, v154
	v_cvt_pk_bf16_f32 v10, v12, v13
	v_mul_f32_e32 v12, v194, v158
	v_mul_f32_e32 v13, v195, v162
	v_cvt_pk_bf16_f32 v11, v12, v13
	ds_write_b128 v5, v[8:11] offset:1024
	v_mul_f32_e32 v12, v188, v135
	v_mul_f32_e32 v13, v189, v139
	v_cvt_pk_bf16_f32 v8, v12, v13
	v_mul_f32_e32 v12, v190, v143
	v_mul_f32_e32 v13, v191, v147
	v_cvt_pk_bf16_f32 v9, v12, v13
	v_mul_f32_e32 v12, v192, v151
	v_mul_f32_e32 v13, v193, v155
	v_cvt_pk_bf16_f32 v10, v12, v13
	v_mul_f32_e32 v12, v194, v159
	v_mul_f32_e32 v13, v195, v163
	v_cvt_pk_bf16_f32 v11, v12, v13
	ds_write_b128 v5, v[8:11] offset:1536
	s_waitcnt lgkmcnt(0)
	s_barrier
; #define LAS __attribute__((address_space(3)))
; #define GAS __attribute__((address_space(1)))
; #define SB() __builtin_amdgcn_sched_barrier(0)
; #define LDS_WAIT() asm volatile("s_waitcnt lgkmcnt(0)" ::: "memory")
; __device__ __forceinline__ void wg_convert_tile(Frame& F, const float* W, int ldw, bf16_t* WT, int Kd, int k0, int n0, int kind, const float* kgain) {
;     ...
;     LDS_WAIT(); __syncthreads();
; #pragma unroll
;     for (int t = 0; t < 16; t += 4) { u32x4 v[4];
; #pragma unroll
;         for (int q = 0; q < 4; ++q) { const int idx = (t + q) * 512 + w * 64 + lane, n = idx >> 5, kc = idx & 31; v[q] = *(const LAS u32x4*)(img + n * 512 + ((kc ^ ((n >> 2) & 31)) << 4)); }
;         SB();
; #pragma unroll
;         for (int q = 0; q < 4; ++q) { const int idx = (t + q) * 512 + w * 64 + lane, n = idx >> 5, kc = idx & 31, nn = n0 + n;
;             const int row = kind < 0 ? nn : ((nn >> 7) * 256 + kind * 128 + (nn & 127));
;             __builtin_nontemporal_store(v[q], (GAS u32x4*)(WT + (size_t)row * Kd + k0 + 8 * kc)); }
;         SB(); }
;     LDS_WAIT(); __syncthreads();
	v_lshlrev_b32_e32 v18, 9, v16
	s_lshr_b32 s83, s8, 1
	s_add_i32 s98, s83, 0
	s_and_b32 s98, s98, 31
	v_xor_b32_e32 v7, s98, v14
	v_lshlrev_b32_e32 v7, 4, v7
	s_mov_b32 s99, 0
	v_add3_u32 v7, v7, v18, s99
	ds_read_b128 v[20:23], v7
	s_add_i32 s98, s83, 4
	s_and_b32 s98, s98, 31
	v_xor_b32_e32 v7, s98, v14
	v_lshlrev_b32_e32 v7, 4, v7
	s_mov_b32 s99, 8192
	v_add3_u32 v7, v7, v18, s99
	ds_read_b128 v[24:27], v7
	s_add_i32 s98, s83, 8
	s_and_b32 s98, s98, 31
	v_xor_b32_e32 v7, s98, v14
	v_lshlrev_b32_e32 v7, 4, v7
	s_mov_b32 s99, 16384
	v_add3_u32 v7, v7, v18, s99
	ds_read_b128 v[28:31], v7
	s_add_i32 s98, s83, 12
	s_and_b32 s98, s98, 31
	v_xor_b32_e32 v7, s98, v14
	v_lshlrev_b32_e32 v7, 4, v7
	s_mov_b32 s99, 24576
	v_add3_u32 v7, v7, v18, s99
	ds_read_b128 v[32:35], v7
	s_waitcnt lgkmcnt(0)
	s_movk_i32 s98, 0
	s_mul_i32 s98, s98, s55
	s_add_u32 s98, s64, s98
	s_addc_u32 s99, s65, 0
	global_store_dwordx4 v6, v[20:23], s[98:99] nt
	s_movk_i32 s98, 16
	s_mul_i32 s98, s98, s55
	s_add_u32 s98, s64, s98
	s_addc_u32 s99, s65, 0
	global_store_dwordx4 v6, v[24:27], s[98:99] nt
	s_movk_i32 s98, 32
	s_mul_i32 s98, s98, s55
	s_add_u32 s98, s64, s98
	s_addc_u32 s99, s65, 0
	global_store_dwordx4 v6, v[28:31], s[98:99] nt
	s_movk_i32 s98, 48
	s_mul_i32 s98, s98, s55
	s_add_u32 s98, s64, s98
	s_addc_u32 s99, s65, 0
	global_store_dwordx4 v6, v[32:35], s[98:99] nt
	s_add_i32 s98, s83, 16
	s_and_b32 s98, s98, 31
	v_xor_b32_e32 v7, s98, v14
	v_lshlrev_b32_e32 v7, 4, v7
	s_mov_b32 s99, 32768
	v_add3_u32 v7, v7, v18, s99
	ds_read_b128 v[20:23], v7
	s_add_i32 s98, s83, 20
	s_and_b32 s98, s98, 31
	v_xor_b32_e32 v7, s98, v14
	v_lshlrev_b32_e32 v7, 4, v7
	s_mov_b32 s99, 40960
	v_add3_u32 v7, v7, v18, s99
	ds_read_b128 v[24:27], v7
	s_add_i32 s98, s83, 24
	s_and_b32 s98, s98, 31
	v_xor_b32_e32 v7, s98, v14
	v_lshlrev_b32_e32 v7, 4, v7
	s_mov_b32 s99, 49152
	v_add3_u32 v7, v7, v18, s99
	ds_read_b128 v[28:31], v7
	s_add_i32 s98, s83, 28
	s_and_b32 s98, s98, 31
	v_xor_b32_e32 v7, s98, v14
	v_lshlrev_b32_e32 v7, 4, v7
	s_mov_b32 s99, 57344
	v_add3_u32 v7, v7, v18, s99
	ds_read_b128 v[32:35], v7
	s_waitcnt lgkmcnt(0)
	s_movk_i32 s98, 64
	s_mul_i32 s98, s98, s55
	s_add_u32 s98, s64, s98
	s_addc_u32 s99, s65, 0
	global_store_dwordx4 v6, v[20:23], s[98:99] nt
	s_movk_i32 s98, 80
	s_mul_i32 s98, s98, s55
	s_add_u32 s98, s64, s98
	s_addc_u32 s99, s65, 0
	global_store_dwordx4 v6, v[24:27], s[98:99] nt
	s_movk_i32 s98, 96
	s_mul_i32 s98, s98, s55
	s_add_u32 s98, s64, s98
	s_addc_u32 s99, s65, 0
	global_store_dwordx4 v6, v[28:31], s[98:99] nt
	s_movk_i32 s98, 112
	s_mul_i32 s98, s98, s55
	s_add_u32 s98, s64, s98
	s_addc_u32 s99, s65, 0
	global_store_dwordx4 v6, v[32:35], s[98:99] nt
	s_add_i32 s98, s83, 32
	s_and_b32 s98, s98, 31
	v_xor_b32_e32 v7, s98, v14
	v_lshlrev_b32_e32 v7, 4, v7
	s_mov_b32 s99, 65536
	v_add3_u32 v7, v7, v18, s99
	ds_read_b128 v[20:23], v7
	s_add_i32 s98, s83, 36
	s_and_b32 s98, s98, 31
	v_xor_b32_e32 v7, s98, v14
	v_lshlrev_b32_e32 v7, 4, v7
	s_mov_b32 s99, 73728
	v_add3_u32 v7, v7, v18, s99
	ds_read_b128 v[24:27], v7
	s_add_i32 s98, s83, 40
	s_and_b32 s98, s98, 31
	v_xor_b32_e32 v7, s98, v14
	v_lshlrev_b32_e32 v7, 4, v7
	s_mov_b32 s99, 81920
	v_add3_u32 v7, v7, v18, s99
	ds_read_b128 v[28:31], v7
	s_add_i32 s98, s83, 44
	s_and_b32 s98, s98, 31
	v_xor_b32_e32 v7, s98, v14
	v_lshlrev_b32_e32 v7, 4, v7
	s_mov_b32 s99, 90112
	v_add3_u32 v7, v7, v18, s99
	ds_read_b128 v[32:35], v7
	s_waitcnt lgkmcnt(0)
	s_movk_i32 s98, 128
	s_cmp_eq_u32 s67, 1
	s_cselect_b32 s98, 256, s98
	s_mul_i32 s98, s98, s55
	s_add_u32 s98, s64, s98
	s_addc_u32 s99, s65, 0
	global_store_dwordx4 v6, v[20:23], s[98:99] nt
	s_movk_i32 s98, 144
	s_cmp_eq_u32 s67, 1
	s_cselect_b32 s98, 272, s98
	s_mul_i32 s98, s98, s55
	s_add_u32 s98, s64, s98
	s_addc_u32 s99, s65, 0
	global_store_dwordx4 v6, v[24:27], s[98:99] nt
	s_movk_i32 s98, 160
	s_cmp_eq_u32 s67, 1
	s_cselect_b32 s98, 288, s98
	s_mul_i32 s98, s98, s55
	s_add_u32 s98, s64, s98
	s_addc_u32 s99, s65, 0
	global_store_dwordx4 v6, v[28:31], s[98:99] nt
	s_movk_i32 s98, 176
	s_cmp_eq_u32 s67, 1
	s_cselect_b32 s98, 304, s98
	s_mul_i32 s98, s98, s55
	s_add_u32 s98, s64, s98
	s_addc_u32 s99, s65, 0
	global_store_dwordx4 v6, v[32:35], s[98:99] nt
	s_add_i32 s98, s83, 48
	s_and_b32 s98, s98, 31
	v_xor_b32_e32 v7, s98, v14
	v_lshlrev_b32_e32 v7, 4, v7
	s_mov_b32 s99, 98304
	v_add3_u32 v7, v7, v18, s99
	ds_read_b128 v[20:23], v7
	s_add_i32 s98, s83, 52
	s_and_b32 s98, s98, 31
	v_xor_b32_e32 v7, s98, v14
	v_lshlrev_b32_e32 v7, 4, v7
	s_mov_b32 s99, 106496
	v_add3_u32 v7, v7, v18, s99
	ds_read_b128 v[24:27], v7
	s_add_i32 s98, s83, 56
	s_and_b32 s98, s98, 31
	v_xor_b32_e32 v7, s98, v14
	v_lshlrev_b32_e32 v7, 4, v7
	s_mov_b32 s99, 114688
	v_add3_u32 v7, v7, v18, s99
	ds_read_b128 v[28:31], v7
	s_add_i32 s98, s83, 60
	s_and_b32 s98, s98, 31
	v_xor_b32_e32 v7, s98, v14
	v_lshlrev_b32_e32 v7, 4, v7
	s_mov_b32 s99, 122880
	v_add3_u32 v7, v7, v18, s99
	ds_read_b128 v[32:35], v7
	s_waitcnt lgkmcnt(0)
	s_movk_i32 s98, 192
	s_cmp_eq_u32 s67, 1
	s_cselect_b32 s98, 320, s98
	s_mul_i32 s98, s98, s55
	s_add_u32 s98, s64, s98
	s_addc_u32 s99, s65, 0
	global_store_dwordx4 v6, v[20:23], s[98:99] nt
	s_movk_i32 s98, 208
	s_cmp_eq_u32 s67, 1
	s_cselect_b32 s98, 336, s98
	s_mul_i32 s98, s98, s55
	s_add_u32 s98, s64, s98
	s_addc_u32 s99, s65, 0
	global_store_dwordx4 v6, v[24:27], s[98:99] nt
	s_movk_i32 s98, 224
	s_cmp_eq_u32 s67, 1
	s_cselect_b32 s98, 352, s98
	s_mul_i32 s98, s98, s55
	s_add_u32 s98, s64, s98
	s_addc_u32 s99, s65, 0
	global_store_dwordx4 v6, v[28:31], s[98:99] nt
	s_movk_i32 s98, 240
	s_cmp_eq_u32 s67, 1
	s_cselect_b32 s98, 368, s98
	s_mul_i32 s98, s98, s55
	s_add_u32 s98, s64, s98
	s_addc_u32 s99, s65, 0
	global_store_dwordx4 v6, v[32:35], s[98:99] nt
	s_add_i32 s101, s101, 1
	s_add_i32 s11, s11, -1
	s_cmp_lg_u32 s11, 0
	s_cbranch_scc1 .Lcv_item
	s_waitcnt vmcnt(0)
	s_barrier
	v_readlane_b32 s6, v253, 0
	v_readlane_b32 s7, v253, 1
	v_readlane_b32 s8, v253, 2
	v_readlane_b32 s9, v253, 3
	v_readlane_b32 s11, v253, 4
	v_readlane_b32 s12, v253, 5
	v_readlane_b32 s13, v253, 6
	v_readlane_b32 s14, v253, 7
	v_readlane_b32 s32, v253, 8
	v_readlane_b32 s38, v253, 9
	v_readlane_b32 s39, v253, 10
	v_readlane_b32 s55, v253, 11
	v_readlane_b32 s56, v253, 12
	v_readlane_b32 s57, v253, 13
	v_readlane_b32 s58, v253, 14
	v_readlane_b32 s59, v253, 15
	v_readlane_b32 s60, v253, 16
	v_readlane_b32 s61, v253, 17
	v_readlane_b32 s62, v253, 18
	v_readlane_b32 s63, v253, 19
	v_readlane_b32 s64, v253, 20
	v_readlane_b32 s65, v253, 21
	v_readlane_b32 s67, v253, 22
	v_readlane_b32 s70, v253, 23
	v_readlane_b32 s71, v253, 24
	v_readlane_b32 s76, v253, 25
	v_readlane_b32 s80, v253, 26
	v_readlane_b32 s81, v253, 27
	v_readlane_b32 s83, v253, 28
	v_readlane_b32 s95, v253, 29
	v_readlane_b32 s96, v253, 30
	v_readlane_b32 s97, v253, 31
	v_readlane_b32 s98, v253, 32
	v_readlane_b32 s99, v253, 33
	s_nop 7
	s_cmp_eq_u32 s100, 0
	s_cbranch_scc1 .Lcv_ret_top
	s_branch .Lcv_ret_bot

; __global__ void __launch_bounds__(NTHR, 2) mega_fwd(Args args) {
	.amdhsa_kernel _ZN2mk8mega_fwdENS_4ArgsE
		.amdhsa_group_segment_fixed_size 0
		.amdhsa_private_segment_fixed_size 0
		.amdhsa_kernarg_size 496
		.amdhsa_user_sgpr_count 2
		.amdhsa_user_sgpr_dispatch_ptr 0
		.amdhsa_user_sgpr_queue_ptr 0
		.amdhsa_user_sgpr_kernarg_segment_ptr 1
		.amdhsa_user_sgpr_dispatch_id 0
		.amdhsa_user_sgpr_kernarg_preload_length 0
		.amdhsa_user_sgpr_kernarg_preload_offset 0
		.amdhsa_user_sgpr_private_segment_size 0
		.amdhsa_uses_dynamic_stack 0
		.amdhsa_enable_private_segment 0
		.amdhsa_system_sgpr_workgroup_id_x 1
		.amdhsa_system_sgpr_workgroup_id_y 0
		.amdhsa_system_sgpr_workgroup_id_z 0
		.amdhsa_system_sgpr_workgroup_info 0
		.amdhsa_system_vgpr_workitem_id 0
		.amdhsa_next_free_vgpr 256
		.amdhsa_next_free_sgpr 102
		.amdhsa_accum_offset 256
		.amdhsa_reserve_vcc 1
		.amdhsa_float_round_mode_32 0
		.amdhsa_float_round_mode_16_64 0
		.amdhsa_float_denorm_mode_32 3
		.amdhsa_float_denorm_mode_16_64 3
		.amdhsa_dx10_clamp 1
		.amdhsa_ieee_mode 1
		.amdhsa_fp16_overflow 0
		.amdhsa_tg_split 0
		.amdhsa_exception_fp_ieee_invalid_op 0
		.amdhsa_exception_fp_denorm_src 0
		.amdhsa_exception_fp_ieee_div_zero 0
		.amdhsa_exception_fp_ieee_overflow 0
		.amdhsa_exception_fp_ieee_underflow 0
		.amdhsa_exception_fp_ieee_inexact 0
		.amdhsa_exception_int_div_zero 0
	.end_amdhsa_kernel

; __global__ void __launch_bounds__(NTHR, 2) mega_fwd(Args args) {
amdhsa.kernels:
  - .agpr_count:     0
    .args:
      - .offset:         0
        .size:           240
        .value_kind:     by_value
      - .offset:         240
        .size:           4
        .value_kind:     hidden_block_count_x
      - .offset:         244
        .size:           4
        .value_kind:     hidden_block_count_y
      - .offset:         248
        .size:           4
        .value_kind:     hidden_block_count_z
      - .offset:         252
        .size:           2
        .value_kind:     hidden_group_size_x
      - .offset:         254
        .size:           2
        .value_kind:     hidden_group_size_y
      - .offset:         256
        .size:           2
        .value_kind:     hidden_group_size_z
      - .offset:         258
        .size:           2
        .value_kind:     hidden_remainder_x
      - .offset:         260
        .size:           2
        .value_kind:     hidden_remainder_y
      - .offset:         262
        .size:           2
        .value_kind:     hidden_remainder_z
      - .offset:         280
        .size:           8
        .value_kind:     hidden_global_offset_x
      - .offset:         288
        .size:           8
        .value_kind:     hidden_global_offset_y
      - .offset:         296
        .size:           8
        .value_kind:     hidden_global_offset_z
      - .offset:         304
        .size:           2
        .value_kind:     hidden_grid_dims
      - .offset:         360
        .size:           4
        .value_kind:     hidden_dynamic_lds_size
    .group_segment_fixed_size: 0
    .kernarg_segment_align: 8
    .kernarg_segment_size: 496
    .language:       OpenCL C
    .language_version:
      - 2
      - 0
    .max_flat_workgroup_size: 512
    .name:           _ZN2mk8mega_fwdENS_4ArgsE
    .private_segment_fixed_size: 0
    .sgpr_count:     108
    .sgpr_spill_count: 309
    .symbol:         _ZN2mk8mega_fwdENS_4ArgsE.kd
    .uniform_work_group_size: 1
    .uses_dynamic_stack: false
    .vgpr_count:     256
    .vgpr_spill_count: 0
    .wavefront_size: 64
